# flush block of main_kernel hand-rescheduled: LDS fragment prefetch with counted lgkmcnt, 16-wide independent sigmoid chains instead of serial chain; same math
# speedup vs baseline: 1.0335x; 1.0335x over previous
.LBB1_153:
	s_or_b64 exec, exec, s[2:3]
	v_cmp_ge_i32_e32 vcc, s18, v249
	s_mov_b64 s[8:9], 0
	s_and_saveexec_b64 s[2:3], vcc
	s_cbranch_execz .LBB1_148
	v_cmp_gt_i32_e32 vcc, s12, v235
	s_and_b64 s[10:11], s[0:1], vcc
	ds_read_b128 v[82:85], v245 offset:32768
	ds_read_b128 v[86:89], v245 offset:32784
	ds_read_b128 v[90:93], v245 offset:32800
	ds_read_b128 v[94:97], v245 offset:32816
	ds_read_b128 v[98:101], v245 offset:32832
	ds_read_b128 v[102:105], v245 offset:32848
	ds_read_b128 v[106:109], v245 offset:32864
	ds_read_b128 v[110:113], v245 offset:32880
	ds_read_b128 v[114:117], v246 offset:0
	ds_read_b128 v[118:121], v246 offset:8192
	ds_read_b128 v[122:125], v246 offset:1024
	ds_read_b128 v[126:129], v246 offset:9216
	v_cvt_f32_i32_e32 v16, v234
	v_cvt_pk_f16_f32 v4, v66, v67
	v_cvt_pk_f16_f32 v5, v68, v69
	v_cvt_pk_f16_f32 v6, v70, v71
	v_cvt_pk_f16_f32 v7, v72, v73
	v_cvt_pk_f16_f32 v8, v74, v75
	v_cvt_pk_f16_f32 v9, v76, v77
	v_cvt_pk_f16_f32 v10, v78, v79
	v_cvt_pk_f16_f32 v11, v80, v81
	s_waitcnt lgkmcnt(4)
	v_pk_mul_f32 v[162:163], v[82:83], v[16:17] op_sel_hi:[1,0]
	v_pk_mul_f32 v[164:165], v[84:85], v[16:17] op_sel_hi:[1,0]
	v_pk_mul_f32 v[166:167], v[86:87], v[16:17] op_sel_hi:[1,0]
	v_pk_mul_f32 v[168:169], v[88:89], v[16:17] op_sel_hi:[1,0]
	v_pk_mul_f32 v[170:171], v[90:91], v[16:17] op_sel_hi:[1,0]
	v_pk_mul_f32 v[172:173], v[92:93], v[16:17] op_sel_hi:[1,0]
	v_pk_mul_f32 v[174:175], v[94:95], v[16:17] op_sel_hi:[1,0]
	v_pk_mul_f32 v[176:177], v[96:97], v[16:17] op_sel_hi:[1,0]
	v_pk_mul_f32 v[146:147], v[98:99], v[16:17] op_sel_hi:[1,0]
	v_pk_mul_f32 v[148:149], v[100:101], v[16:17] op_sel_hi:[1,0]
	v_pk_mul_f32 v[150:151], v[102:103], v[16:17] op_sel_hi:[1,0]
	v_pk_mul_f32 v[152:153], v[104:105], v[16:17] op_sel_hi:[1,0]
	v_pk_mul_f32 v[154:155], v[106:107], v[16:17] op_sel_hi:[1,0]
	v_pk_mul_f32 v[156:157], v[108:109], v[16:17] op_sel_hi:[1,0]
	v_pk_mul_f32 v[158:159], v[110:111], v[16:17] op_sel_hi:[1,0]
	v_pk_mul_f32 v[160:161], v[112:113], v[16:17] op_sel_hi:[1,0]
	ds_read_b128 v[130:133], v246 offset:2048
	ds_read_b128 v[134:137], v246 offset:10240
	ds_read_b128 v[138:141], v246 offset:3072
	ds_read_b128 v[142:145], v246 offset:11264
	s_waitcnt lgkmcnt(4)
	v_mfma_f32_32x32x16_f16 v[162:177], v[114:117], v[4:7], v[162:177]
	v_mfma_f32_32x32x16_f16 v[146:161], v[118:121], v[4:7], v[146:161]
	v_mfma_f32_32x32x16_f16 v[162:177], v[122:125], v[8:11], v[162:177]
	v_mfma_f32_32x32x16_f16 v[146:161], v[126:129], v[8:11], v[146:161]
	ds_read_b128 v[82:85], v246 offset:4096
	ds_read_b128 v[86:89], v246 offset:12288
	ds_read_b128 v[90:93], v246 offset:5120
	ds_read_b128 v[94:97], v246 offset:13312
	v_cvt_pk_f16_f32 v12, v50, v51
	v_cvt_pk_f16_f32 v13, v52, v53
	v_cvt_pk_f16_f32 v14, v54, v55
	v_cvt_pk_f16_f32 v15, v56, v57
	v_cvt_pk_f16_f32 v252, v58, v59
	v_cvt_pk_f16_f32 v253, v60, v61
	v_cvt_pk_f16_f32 v254, v62, v63
	v_cvt_pk_f16_f32 v255, v64, v65
	s_waitcnt lgkmcnt(4)
	v_mfma_f32_32x32x16_f16 v[162:177], v[130:133], v[12:15], v[162:177]
	v_mfma_f32_32x32x16_f16 v[146:161], v[134:137], v[12:15], v[146:161]
	v_mfma_f32_32x32x16_f16 v[162:177], v[138:141], v[252:255], v[162:177]
	v_mfma_f32_32x32x16_f16 v[146:161], v[142:145], v[252:255], v[146:161]
	ds_read_b128 v[98:101], v246 offset:6144
	ds_read_b128 v[102:105], v246 offset:14336
	ds_read_b128 v[106:109], v246 offset:7168
	ds_read_b128 v[110:113], v246 offset:15360
	v_cvt_pk_f16_f32 v4, v34, v35
	v_cvt_pk_f16_f32 v5, v36, v37
	v_cvt_pk_f16_f32 v6, v38, v39
	v_cvt_pk_f16_f32 v7, v40, v41
	v_cvt_pk_f16_f32 v8, v42, v43
	v_cvt_pk_f16_f32 v9, v44, v45
	v_cvt_pk_f16_f32 v10, v46, v47
	v_cvt_pk_f16_f32 v11, v48, v49
	s_waitcnt lgkmcnt(4)
	v_mfma_f32_32x32x16_f16 v[162:177], v[82:85], v[4:7], v[162:177]
	v_mfma_f32_32x32x16_f16 v[146:161], v[86:89], v[4:7], v[146:161]
	v_mfma_f32_32x32x16_f16 v[162:177], v[90:93], v[8:11], v[162:177]
	v_mfma_f32_32x32x16_f16 v[146:161], v[94:97], v[8:11], v[146:161]
	v_cvt_pk_f16_f32 v12, v18, v19
	v_cvt_pk_f16_f32 v13, v20, v21
	v_cvt_pk_f16_f32 v14, v22, v23
	v_cvt_pk_f16_f32 v15, v24, v25
	v_cvt_pk_f16_f32 v252, v26, v27
	v_cvt_pk_f16_f32 v253, v28, v29
	v_cvt_pk_f16_f32 v254, v30, v31
	v_cvt_pk_f16_f32 v255, v32, v33
	ds_read_b128 v[18:21], v246 offset:16384
	ds_read_b128 v[22:25], v246 offset:20480
	ds_read_b128 v[26:29], v246 offset:24576
	ds_read_b128 v[30:33], v246 offset:28672
	s_waitcnt lgkmcnt(4)
	v_mfma_f32_32x32x16_f16 v[162:177], v[98:101], v[12:15], v[162:177]
	v_mfma_f32_32x32x16_f16 v[146:161], v[102:105], v[12:15], v[146:161]
	v_mfma_f32_32x32x16_f16 v[162:177], v[106:109], v[252:255], v[162:177]
	v_mfma_f32_32x32x16_f16 v[146:161], v[110:113], v[252:255], v[146:161]
	ds_read_b128 v[130:133], v247 offset:33024
	ds_read_b128 v[134:137], v247 offset:33040
	ds_read_b128 v[138:141], v247 offset:33056
	ds_read_b128 v[142:145], v247 offset:33072
	ds_read_b128 v[114:117], v247 offset:33088
	ds_read_b128 v[118:121], v247 offset:33104
	ds_read_b128 v[122:125], v247 offset:33120
	ds_read_b128 v[126:129], v247 offset:33136
	s_nop 2
	v_cvt_pk_f16_f32 v4, v162, v163
	v_cvt_pk_f16_f32 v5, v164, v165
	v_cvt_pk_f16_f32 v6, v166, v167
	v_cvt_pk_f16_f32 v7, v168, v169
	v_cvt_pk_f16_f32 v8, v170, v171
	v_cvt_pk_f16_f32 v9, v172, v173
	v_cvt_pk_f16_f32 v10, v174, v175
	v_cvt_pk_f16_f32 v11, v176, v177
	s_waitcnt lgkmcnt(4)
	ds_read_b128 v[98:101], v247 offset:33152
	ds_read_b128 v[102:105], v247 offset:33168
	ds_read_b128 v[106:109], v247 offset:33184
	ds_read_b128 v[110:113], v247 offset:33200
	ds_read_b128 v[82:85], v247 offset:33216
	ds_read_b128 v[86:89], v247 offset:33232
	ds_read_b128 v[90:93], v247 offset:33248
	ds_read_b128 v[94:97], v247 offset:33264
	v_mfma_f32_32x32x16_f16 v[130:145], v[18:21], v[4:7], v[130:145]
	s_waitcnt lgkmcnt(8)
	v_mfma_f32_32x32x16_f16 v[114:129], v[22:25], v[4:7], v[114:129]
	ds_read_b128 v[34:37], v246 offset:17408
	ds_read_b128 v[38:41], v246 offset:21504
	ds_read_b128 v[42:45], v246 offset:25600
	ds_read_b128 v[46:49], v246 offset:29696
	s_waitcnt lgkmcnt(8)
	v_mfma_f32_32x32x16_f16 v[98:113], v[26:29], v[4:7], v[98:113]
	s_waitcnt lgkmcnt(4)
	v_mfma_f32_32x32x16_f16 v[82:97], v[30:33], v[4:7], v[82:97]
	ds_read_b128 v[50:53], v246 offset:18432
	ds_read_b128 v[54:57], v246 offset:22528
	ds_read_b128 v[58:61], v246 offset:26624
	ds_read_b128 v[62:65], v246 offset:30720
	v_cvt_pk_f16_f32 v12, v146, v147
	v_cvt_pk_f16_f32 v13, v148, v149
	v_cvt_pk_f16_f32 v14, v150, v151
	v_cvt_pk_f16_f32 v15, v152, v153
	v_cvt_pk_f16_f32 v252, v154, v155
	v_cvt_pk_f16_f32 v253, v156, v157
	v_cvt_pk_f16_f32 v254, v158, v159
	v_cvt_pk_f16_f32 v255, v160, v161
	s_waitcnt lgkmcnt(4)
	v_mfma_f32_32x32x16_f16 v[130:145], v[34:37], v[8:11], v[130:145]
	v_mfma_f32_32x32x16_f16 v[114:129], v[38:41], v[8:11], v[114:129]
	v_mfma_f32_32x32x16_f16 v[98:113], v[42:45], v[8:11], v[98:113]
	v_mfma_f32_32x32x16_f16 v[82:97], v[46:49], v[8:11], v[82:97]
	ds_read_b128 v[66:69], v246 offset:19456
	ds_read_b128 v[70:73], v246 offset:23552
	ds_read_b128 v[74:77], v246 offset:27648
	ds_read_b128 v[78:81], v246 offset:31744
	s_waitcnt lgkmcnt(4)
	v_mfma_f32_32x32x16_f16 v[130:145], v[50:53], v[12:15], v[130:145]
	v_mfma_f32_32x32x16_f16 v[114:129], v[54:57], v[12:15], v[114:129]
	v_mfma_f32_32x32x16_f16 v[98:113], v[58:61], v[12:15], v[98:113]
	v_mfma_f32_32x32x16_f16 v[82:97], v[62:65], v[12:15], v[82:97]
	ds_read_b128 v[146:149], v247 offset:33536
	ds_read_b128 v[150:153], v247 offset:33552
	ds_read_b128 v[154:157], v247 offset:33568
	ds_read_b128 v[158:161], v247 offset:33584
	ds_read_b128 v[162:165], v247 offset:33600
	ds_read_b128 v[166:169], v247 offset:33616
	ds_read_b128 v[170:173], v247 offset:33632
	ds_read_b128 v[174:177], v247 offset:33648
	s_waitcnt lgkmcnt(8)
	v_mfma_f32_32x32x16_f16 v[130:145], v[66:69], v[252:255], v[130:145]
	v_mfma_f32_32x32x16_f16 v[114:129], v[70:73], v[252:255], v[114:129]
	v_mfma_f32_32x32x16_f16 v[98:113], v[74:77], v[252:255], v[98:113]
	v_mfma_f32_32x32x16_f16 v[82:97], v[78:81], v[252:255], v[82:97]
	ds_read_b128 v[18:21], v247 offset:33664
	ds_read_b128 v[22:25], v247 offset:33680
	ds_read_b128 v[26:29], v247 offset:33696
	ds_read_b128 v[30:33], v247 offset:33712
	s_nop 4
	v_exp_f32_e32 v130, v130
	v_exp_f32_e32 v131, v131
	v_exp_f32_e32 v132, v132
	v_exp_f32_e32 v133, v133
	v_exp_f32_e32 v134, v134
	v_exp_f32_e32 v135, v135
	v_exp_f32_e32 v136, v136
	v_exp_f32_e32 v137, v137
	v_exp_f32_e32 v138, v138
	v_exp_f32_e32 v139, v139
	v_exp_f32_e32 v140, v140
	v_exp_f32_e32 v141, v141
	v_exp_f32_e32 v142, v142
	v_exp_f32_e32 v143, v143
	v_exp_f32_e32 v144, v144
	v_exp_f32_e32 v145, v145
	s_waitcnt lgkmcnt(8)
	ds_read_b128 v[34:37], v247 offset:33728
	ds_read_b128 v[38:41], v247 offset:33744
	ds_read_b128 v[42:45], v247 offset:33760
	ds_read_b128 v[46:49], v247 offset:33776
	v_add_f32_e32 v130, 1.0, v130
	v_add_f32_e32 v131, 1.0, v131
	v_add_f32_e32 v132, 1.0, v132
	v_add_f32_e32 v133, 1.0, v133
	v_add_f32_e32 v134, 1.0, v134
	v_add_f32_e32 v135, 1.0, v135
	v_add_f32_e32 v136, 1.0, v136
	v_add_f32_e32 v137, 1.0, v137
	v_add_f32_e32 v138, 1.0, v138
	v_add_f32_e32 v139, 1.0, v139
	v_add_f32_e32 v140, 1.0, v140
	v_add_f32_e32 v141, 1.0, v141
	v_add_f32_e32 v142, 1.0, v142
	v_add_f32_e32 v143, 1.0, v143
	v_add_f32_e32 v144, 1.0, v144
	v_add_f32_e32 v145, 1.0, v145
	v_rcp_f32_e32 v130, v130
	v_rcp_f32_e32 v131, v131
	v_rcp_f32_e32 v132, v132
	v_rcp_f32_e32 v133, v133
	v_rcp_f32_e32 v134, v134
	v_rcp_f32_e32 v135, v135
	v_rcp_f32_e32 v136, v136
	v_rcp_f32_e32 v137, v137
	v_rcp_f32_e32 v138, v138
	v_rcp_f32_e32 v139, v139
	v_rcp_f32_e32 v140, v140
	v_rcp_f32_e32 v141, v141
	v_rcp_f32_e32 v142, v142
	v_rcp_f32_e32 v143, v143
	v_rcp_f32_e32 v144, v144
	v_rcp_f32_e32 v145, v145
	v_mul_f32_e32 v3, v146, v130
	v_mul_f32_e32 v4, v147, v131
	v_mul_f32_e32 v5, v148, v132
	v_mul_f32_e32 v6, v149, v133
	v_fmac_f32_e32 v3, v150, v134
	v_fmac_f32_e32 v4, v151, v135
	v_fmac_f32_e32 v5, v152, v136
	v_fmac_f32_e32 v6, v153, v137
	v_fmac_f32_e32 v3, v154, v138
	v_fmac_f32_e32 v4, v155, v139
	v_fmac_f32_e32 v5, v156, v140
	v_fmac_f32_e32 v6, v157, v141
	v_fmac_f32_e32 v3, v158, v142
	v_fmac_f32_e32 v4, v159, v143
	v_fmac_f32_e32 v5, v160, v144
	v_fmac_f32_e32 v6, v161, v145
	v_exp_f32_e32 v114, v114
	v_exp_f32_e32 v115, v115
	v_exp_f32_e32 v116, v116
	v_exp_f32_e32 v117, v117
	v_exp_f32_e32 v118, v118
	v_exp_f32_e32 v119, v119
	v_exp_f32_e32 v120, v120
	v_exp_f32_e32 v121, v121
	v_exp_f32_e32 v122, v122
	v_exp_f32_e32 v123, v123
	v_exp_f32_e32 v124, v124
	v_exp_f32_e32 v125, v125
	v_exp_f32_e32 v126, v126
	v_exp_f32_e32 v127, v127
	v_exp_f32_e32 v128, v128
	v_exp_f32_e32 v129, v129
	v_add_f32_e32 v114, 1.0, v114
	v_add_f32_e32 v115, 1.0, v115
	v_add_f32_e32 v116, 1.0, v116
	v_add_f32_e32 v117, 1.0, v117
	v_add_f32_e32 v118, 1.0, v118
	v_add_f32_e32 v119, 1.0, v119
	v_add_f32_e32 v120, 1.0, v120
	v_add_f32_e32 v121, 1.0, v121
	v_add_f32_e32 v122, 1.0, v122
	v_add_f32_e32 v123, 1.0, v123
	v_add_f32_e32 v124, 1.0, v124
	v_add_f32_e32 v125, 1.0, v125
	v_add_f32_e32 v126, 1.0, v126
	v_add_f32_e32 v127, 1.0, v127
	v_add_f32_e32 v128, 1.0, v128
	v_add_f32_e32 v129, 1.0, v129
	v_rcp_f32_e32 v114, v114
	v_rcp_f32_e32 v115, v115
	v_rcp_f32_e32 v116, v116
	v_rcp_f32_e32 v117, v117
	v_rcp_f32_e32 v118, v118
	v_rcp_f32_e32 v119, v119
	v_rcp_f32_e32 v120, v120
	v_rcp_f32_e32 v121, v121
	v_rcp_f32_e32 v122, v122
	v_rcp_f32_e32 v123, v123
	v_rcp_f32_e32 v124, v124
	v_rcp_f32_e32 v125, v125
	v_rcp_f32_e32 v126, v126
	v_rcp_f32_e32 v127, v127
	v_rcp_f32_e32 v128, v128
	v_rcp_f32_e32 v129, v129
	s_waitcnt lgkmcnt(8)
	v_fmac_f32_e32 v3, v162, v114
	v_fmac_f32_e32 v4, v163, v115
	v_fmac_f32_e32 v5, v164, v116
	v_fmac_f32_e32 v6, v165, v117
	v_fmac_f32_e32 v3, v166, v118
	v_fmac_f32_e32 v4, v167, v119
	v_fmac_f32_e32 v5, v168, v120
	v_fmac_f32_e32 v6, v169, v121
	v_fmac_f32_e32 v3, v170, v122
	v_fmac_f32_e32 v4, v171, v123
	v_fmac_f32_e32 v5, v172, v124
	v_fmac_f32_e32 v6, v173, v125
	v_fmac_f32_e32 v3, v174, v126
	v_fmac_f32_e32 v4, v175, v127
	v_fmac_f32_e32 v5, v176, v128
	v_fmac_f32_e32 v6, v177, v129
	v_exp_f32_e32 v98, v98
	v_exp_f32_e32 v99, v99
	v_exp_f32_e32 v100, v100
	v_exp_f32_e32 v101, v101
	v_exp_f32_e32 v102, v102
	v_exp_f32_e32 v103, v103
	v_exp_f32_e32 v104, v104
	v_exp_f32_e32 v105, v105
	v_exp_f32_e32 v106, v106
	v_exp_f32_e32 v107, v107
	v_exp_f32_e32 v108, v108
	v_exp_f32_e32 v109, v109
	v_exp_f32_e32 v110, v110
	v_exp_f32_e32 v111, v111
	v_exp_f32_e32 v112, v112
	v_exp_f32_e32 v113, v113
	v_add_f32_e32 v98, 1.0, v98
	v_add_f32_e32 v99, 1.0, v99
	v_add_f32_e32 v100, 1.0, v100
	v_add_f32_e32 v101, 1.0, v101
	v_add_f32_e32 v102, 1.0, v102
	v_add_f32_e32 v103, 1.0, v103
	v_add_f32_e32 v104, 1.0, v104
	v_add_f32_e32 v105, 1.0, v105
	v_add_f32_e32 v106, 1.0, v106
	v_add_f32_e32 v107, 1.0, v107
	v_add_f32_e32 v108, 1.0, v108
	v_add_f32_e32 v109, 1.0, v109
	v_add_f32_e32 v110, 1.0, v110
	v_add_f32_e32 v111, 1.0, v111
	v_add_f32_e32 v112, 1.0, v112
	v_add_f32_e32 v113, 1.0, v113
	v_rcp_f32_e32 v98, v98
	v_rcp_f32_e32 v99, v99
	v_rcp_f32_e32 v100, v100
	v_rcp_f32_e32 v101, v101
	v_rcp_f32_e32 v102, v102
	v_rcp_f32_e32 v103, v103
	v_rcp_f32_e32 v104, v104
	v_rcp_f32_e32 v105, v105
	v_rcp_f32_e32 v106, v106
	v_rcp_f32_e32 v107, v107
	v_rcp_f32_e32 v108, v108
	v_rcp_f32_e32 v109, v109
	v_rcp_f32_e32 v110, v110
	v_rcp_f32_e32 v111, v111
	v_rcp_f32_e32 v112, v112
	v_rcp_f32_e32 v113, v113
	s_waitcnt lgkmcnt(4)
	v_fmac_f32_e32 v3, v18, v98
	v_fmac_f32_e32 v4, v19, v99
	v_fmac_f32_e32 v5, v20, v100
	v_fmac_f32_e32 v6, v21, v101
	v_fmac_f32_e32 v3, v22, v102
	v_fmac_f32_e32 v4, v23, v103
	v_fmac_f32_e32 v5, v24, v104
	v_fmac_f32_e32 v6, v25, v105
	v_fmac_f32_e32 v3, v26, v106
	v_fmac_f32_e32 v4, v27, v107
	v_fmac_f32_e32 v5, v28, v108
	v_fmac_f32_e32 v6, v29, v109
	v_fmac_f32_e32 v3, v30, v110
	v_fmac_f32_e32 v4, v31, v111
	v_fmac_f32_e32 v5, v32, v112
	v_fmac_f32_e32 v6, v33, v113
	v_exp_f32_e32 v82, v82
	v_exp_f32_e32 v83, v83
	v_exp_f32_e32 v84, v84
	v_exp_f32_e32 v85, v85
	v_exp_f32_e32 v86, v86
	v_exp_f32_e32 v87, v87
	v_exp_f32_e32 v88, v88
	v_exp_f32_e32 v89, v89
	v_exp_f32_e32 v90, v90
	v_exp_f32_e32 v91, v91
	v_exp_f32_e32 v92, v92
	v_exp_f32_e32 v93, v93
	v_exp_f32_e32 v94, v94
	v_exp_f32_e32 v95, v95
	v_exp_f32_e32 v96, v96
	v_exp_f32_e32 v97, v97
	v_add_f32_e32 v82, 1.0, v82
	v_add_f32_e32 v83, 1.0, v83
	v_add_f32_e32 v84, 1.0, v84
	v_add_f32_e32 v85, 1.0, v85
	v_add_f32_e32 v86, 1.0, v86
	v_add_f32_e32 v87, 1.0, v87
	v_add_f32_e32 v88, 1.0, v88
	v_add_f32_e32 v89, 1.0, v89
	v_add_f32_e32 v90, 1.0, v90
	v_add_f32_e32 v91, 1.0, v91
	v_add_f32_e32 v92, 1.0, v92
	v_add_f32_e32 v93, 1.0, v93
	v_add_f32_e32 v94, 1.0, v94
	v_add_f32_e32 v95, 1.0, v95
	v_add_f32_e32 v96, 1.0, v96
	v_add_f32_e32 v97, 1.0, v97
	v_rcp_f32_e32 v82, v82
	v_rcp_f32_e32 v83, v83
	v_rcp_f32_e32 v84, v84
	v_rcp_f32_e32 v85, v85
	v_rcp_f32_e32 v86, v86
	v_rcp_f32_e32 v87, v87
	v_rcp_f32_e32 v88, v88
	v_rcp_f32_e32 v89, v89
	v_rcp_f32_e32 v90, v90
	v_rcp_f32_e32 v91, v91
	v_rcp_f32_e32 v92, v92
	v_rcp_f32_e32 v93, v93
	v_rcp_f32_e32 v94, v94
	v_rcp_f32_e32 v95, v95
	v_rcp_f32_e32 v96, v96
	v_rcp_f32_e32 v97, v97
	s_waitcnt lgkmcnt(0)
	v_fmac_f32_e32 v3, v34, v82
	v_fmac_f32_e32 v4, v35, v83
	v_fmac_f32_e32 v5, v36, v84
	v_fmac_f32_e32 v6, v37, v85
	v_fmac_f32_e32 v3, v38, v86
	v_fmac_f32_e32 v4, v39, v87
	v_fmac_f32_e32 v5, v40, v88
	v_fmac_f32_e32 v6, v41, v89
	v_fmac_f32_e32 v3, v42, v90
	v_fmac_f32_e32 v4, v43, v91
	v_fmac_f32_e32 v5, v44, v92
	v_fmac_f32_e32 v6, v45, v93
	v_fmac_f32_e32 v3, v46, v94
	v_fmac_f32_e32 v4, v47, v95
	v_fmac_f32_e32 v5, v48, v96
	v_fmac_f32_e32 v6, v49, v97
	v_add_f32_e32 v3, v3, v4
	v_add_f32_e32 v5, v5, v6
	v_add_f32_e32 v3, v3, v5
	ds_bpermute_b32 v4, v248, v3
	s_and_saveexec_b64 s[8:9], s[10:11]
	s_cbranch_execz .LBB1_156
	s_waitcnt vmcnt(0)
	v_mul_f32_e32 v5, 0x40549a78, v238
	v_exp_f32_e32 v5, v5
	s_waitcnt lgkmcnt(0)
	v_add_f32_e32 v3, v3, v4
	v_ashrrev_i32_e32 v7, 31, v235
	v_mov_b32_e32 v6, v235
	v_add_f32_e32 v3, v239, v3
	v_lshl_add_u64 v[6:7], v[6:7], 2, s[52:53]
	v_mul_f32_e32 v3, v5, v3
	global_store_dword v[6:7], v3, off
